# RG-LRU phase: one static s_setprio 1 for waves 4-7 (reset to 0 at the end of the phase)
# speedup vs baseline: 1.0067x; 1.0067x over previous
.LBB0_1451:
	s_load_dwordx4 s[0:3], s[8:9], 0x138
	s_waitcnt lgkmcnt(0)
	s_mov_b64 s[4:5], s[0:1]
	s_cmp_lt_i32 s4, 12
	s_cselect_b64 s[0:1], -1, 0
	s_cmp_gt_i32 s5, 11
	s_cselect_b64 s[2:3], -1, 0
	s_and_b64 s[0:1], s[0:1], s[2:3]
	s_andn2_b64 vcc, exec, s[0:1]
	s_cbranch_vccnz .LBB0_1535
	s_mov_b64 s[24:25], s[8:9]
	v_mbcnt_lo_u32_b32 v202, -1, 0
	v_mbcnt_hi_u32_b32 v202, -1, v202
	s_load_dword s0, s[8:9], 0x148
	s_waitcnt lgkmcnt(0)
	v_writelane_b32 v241, s0, 18
	s_nop 1
	v_writelane_b32 v241, s1, 19
	s_add_u32 s0, s8, 0x148
	s_addc_u32 s1, s9, 0
	v_writelane_b32 v241, s0, 34
	s_nop 1
	v_writelane_b32 v241, s1, 35
	v_readlane_b32 s0, v243, 0
	s_cmpk_gt_i32 s0, 0xff
	v_readlane_b32 s1, v243, 1
	s_cbranch_scc1 .LBB0_1482
	v_readlane_b32 s0, v243, 7
	v_readlane_b32 s1, v243, 8
	v_readlane_b32 s4, v243, 0
	v_readlane_b32 s6, v243, 12
	s_load_dwordx2 s[2:3], s[0:1], 0x130
	s_lshr_b32 s7, s6, 2
	s_cmp_ge_u32 s6, 4
	s_cbranch_scc0 .Lmylru_prio
	s_setprio 1
.Lmylru_prio:
	s_and_b32 s8, s6, 3
	s_bfe_u32 s11, s4, 0x20003
	s_lshr_b32 s50, s4, 5
	s_lshl_b32 s50, s50, 3
	s_and_b32 s51, s4, 7
	s_or_b32 s50, s50, s51
	s_lshr_b32 s9, s50, 2
	s_and_b32 s10, s50, 3
	v_and_b32_e32 v160, 15, v202
	v_lshrrev_b32_e32 v161, 4, v202
	v_lshlrev_b32_e32 v209, 2, v202
	s_lshl_b32 s50, s7, 15
	v_xor_b32_e32 v178, v161, v160
	v_lshlrev_b32_e32 v178, 4, v178
	v_lshl_add_u32 v162, v160, 9, v178
	v_add_u32_e32 v162, s50, v162
	s_lshl_b32 s51, s11, 6
	s_lshl_b32 s52, s8, 4
	s_add_i32 s51, s51, s52
	v_add_u32_e32 v179, s51, v160
	v_lshrrev_b32_e32 v180, 3, v179
	v_and_b32_e32 v181, 7, v179
	v_lshlrev_b32_e32 v181, 1, v181
	v_lshlrev_b32_e32 v182, 2, v161
	v_add_u32_e32 v183, 0, v182
	v_xor_b32_e32 v184, v180, v183
	v_lshlrev_b32_e32 v184, 4, v184
	v_lshl_add_u32 v184, v183, 9, v184
	v_add3_u32 v165, v184, v181, s50
	v_add_u32_e32 v183, 1, v182
	v_xor_b32_e32 v184, v180, v183
	v_lshlrev_b32_e32 v184, 4, v184
	v_lshl_add_u32 v184, v183, 9, v184
	v_add3_u32 v166, v184, v181, s50
	v_add_u32_e32 v183, 2, v182
	v_xor_b32_e32 v184, v180, v183
	v_lshlrev_b32_e32 v184, 4, v184
	v_lshl_add_u32 v184, v183, 9, v184
	v_add3_u32 v167, v184, v181, s50
	v_add_u32_e32 v183, 3, v182
	v_xor_b32_e32 v184, v180, v183
	v_lshlrev_b32_e32 v184, 4, v184
	v_lshl_add_u32 v184, v183, 9, v184
	v_add3_u32 v168, v184, v181, s50
	v_lshrrev_b32_e32 v185, 5, v202
	v_and_b32_e32 v186, 31, v202
	s_lshl_b32 s51, s6, 4
	v_add_u32_e32 v187, 0, v185
	v_xor_b32_e32 v188, v186, v187
	v_lshlrev_b32_e32 v188, 4, v188
	v_add_u32_e32 v187, s51, v187
	v_lshl_add_u32 v211, v187, 11, v188
	v_add_u32_e32 v187, 2, v185
	v_xor_b32_e32 v188, v186, v187
	v_lshlrev_b32_e32 v188, 4, v188
	v_add_u32_e32 v187, s51, v187
	v_lshl_add_u32 v212, v187, 11, v188
	v_add_u32_e32 v187, 4, v185
	v_xor_b32_e32 v188, v186, v187
	v_lshlrev_b32_e32 v188, 4, v188
	v_add_u32_e32 v187, s51, v187
	v_lshl_add_u32 v213, v187, 11, v188
	v_add_u32_e32 v187, 6, v185
	v_xor_b32_e32 v188, v186, v187
	v_lshlrev_b32_e32 v188, 4, v188
	v_add_u32_e32 v187, s51, v187
	v_lshl_add_u32 v214, v187, 11, v188
	v_add_u32_e32 v187, 8, v185
	v_xor_b32_e32 v188, v186, v187
	v_lshlrev_b32_e32 v188, 4, v188
	v_add_u32_e32 v187, s51, v187
	v_lshl_add_u32 v215, v187, 11, v188
	v_add_u32_e32 v187, 10, v185
	v_xor_b32_e32 v188, v186, v187
	v_lshlrev_b32_e32 v188, 4, v188
	v_add_u32_e32 v187, s51, v187
	v_lshl_add_u32 v216, v187, 11, v188
	v_add_u32_e32 v187, 12, v185
	v_xor_b32_e32 v188, v186, v187
	v_lshlrev_b32_e32 v188, 4, v188
	v_add_u32_e32 v187, s51, v187
	v_lshl_add_u32 v217, v187, 11, v188
	v_add_u32_e32 v187, 14, v185
	v_xor_b32_e32 v188, v186, v187
	v_lshlrev_b32_e32 v188, 4, v188
	v_add_u32_e32 v187, s51, v187
	v_lshl_add_u32 v218, v187, 11, v188
	s_lshl_b32 s51, s6, 7
	s_add_i32 s51, s51, 0x20000
	v_lshl_add_u32 v207, v160, 3, s51
	s_lshl_b32 s51, s8, 7
	s_add_i32 s51, s51, 0x20000
	v_lshl_add_u32 v208, v160, 3, s51
	s_lshl_b32 s51, s7, 6
	v_add_u32_e32 v189, s51, v182
	s_lshl_b32 s51, s8, 4
	v_add_u32_e32 v190, s51, v160
	v_lshlrev_b32_e32 v190, 1, v190
	v_lshl_add_u32 v210, v189, 11, v190
	s_waitcnt lgkmcnt(0)
	s_lshl_b32 s50, s10, 9
	s_add_u32 s16, s2, s50
	s_addc_u32 s17, s3, 0
	s_add_u32 s16, s16, 0x1b900000
	s_addc_u32 s17, s17, 0
	s_lshl_b32 s50, s10, 9
	s_lshl_b32 s51, s11, 7
	s_add_i32 s50, s50, s51
	s_add_u32 s18, s2, s50
	s_addc_u32 s19, s3, 0
	s_add_u32 s18, s18, 0x13100000
	s_addc_u32 s19, s19, 0
	s_add_u32 s20, s2, s50
	s_addc_u32 s21, s3, 0
	s_add_u32 s20, s20, 0x29100000
	s_addc_u32 s21, s21, 0
	s_lshl_b32 s50, s4, 18
	s_add_u32 s22, s2, s50
	s_addc_u32 s23, s3, 0
	s_add_u32 s22, s22, 0x20100000
	s_addc_u32 s23, s23, 0
	s_lshl_b32 s50, s10, 10
	s_lshl_b32 s51, s11, 6
	s_add_i32 s50, s50, s51
	s_lshl_b32 s51, s8, 4
	s_add_i32 s50, s50, s51
	s_add_i32 s50, s50, 0
	s_lshl_b32 s50, s50, 9
	s_add_u32 s46, s2, s50
	s_addc_u32 s47, s3, 0
	s_add_u32 s46, s46, 0x1000000
	s_addc_u32 s47, s47, 0
	s_add_u32 s48, s46, 0x20000
	s_addc_u32 s49, s47, 0
	v_lshlrev_b32_e32 v178, 9, v160
	v_lshl_add_u32 v178, v161, 4, v178
	global_load_dwordx4 v[0:3], v178, s[46:47]
	global_load_dwordx4 v[4:7], v178, s[46:47] offset:64
	global_load_dwordx4 v[8:11], v178, s[46:47] offset:128
	global_load_dwordx4 v[12:15], v178, s[46:47] offset:192
	global_load_dwordx4 v[16:19], v178, s[46:47] offset:256
	global_load_dwordx4 v[20:23], v178, s[46:47] offset:320
	global_load_dwordx4 v[24:27], v178, s[46:47] offset:384
	global_load_dwordx4 v[28:31], v178, s[46:47] offset:448
	global_load_dwordx4 v[32:35], v178, s[48:49]
	global_load_dwordx4 v[36:39], v178, s[48:49] offset:64
	global_load_dwordx4 v[40:43], v178, s[48:49] offset:128
	global_load_dwordx4 v[44:47], v178, s[48:49] offset:192
	global_load_dwordx4 v[48:51], v178, s[48:49] offset:256
	global_load_dwordx4 v[52:55], v178, s[48:49] offset:320
	global_load_dwordx4 v[56:59], v178, s[48:49] offset:384
	global_load_dwordx4 v[60:63], v178, s[48:49] offset:448
	s_load_dwordx2 s[46:47], s[0:1], 0xa0
	s_load_dwordx2 s[48:49], s[0:1], 0xb0
	s_load_dwordx2 s[40:41], s[0:1], 0xb8
	s_lshl_b32 s50, s10, 8
	s_lshl_b32 s51, s11, 6
	s_add_i32 s50, s50, s51
	s_lshl_b32 s51, s8, 4
	s_add_i32 s50, s50, s51
	v_add_u32_e32 v179, s50, v160
	v_lshlrev_b32_e32 v179, 2, v179
	s_waitcnt lgkmcnt(0)
	global_load_dword v173, v179, s[46:47]
	global_load_dword v174, v179, s[48:49]
	global_load_dword v175, v179, s[40:41]
	v_cmp_le_u32_e64 s[34:35], 16, v202
	v_cmp_le_u32_e64 s[36:37], 32, v202
	v_add_u32_e32 v204, -16, v202
	v_add_u32_e32 v205, -32, v202
	v_add_u32_e32 v206, 48, v160
	s_cmp_eq_u32 s7, 1
	s_cselect_b64 s[38:39], -1, 0
	v_and_b32_e32 v204, 63, v204
	v_lshlrev_b32_e32 v204, 2, v204
	v_and_b32_e32 v205, 63, v205
	v_lshlrev_b32_e32 v205, 2, v205
	v_and_b32_e32 v206, 63, v206
	v_lshlrev_b32_e32 v206, 2, v206
	v_mov_b32_e32 v176, 0
	s_mov_b32 s53, 0xbfb8aa3b
	s_mov_b32 s13, 0
	s_barrier
	s_cmp_lt_u32 s13, 2
	s_lshl_b32 s50, s13, 7
	s_lshl_b32 s51, s9, 8
	s_add_i32 s51, s51, 0x8000
	s_add_i32 s51, s51, s50
	s_lshl_b32 s59, s9, 11
	s_add_i32 s59, s59, s50
	s_addk_i32 s59, 0xff00
	s_cmp_lt_u32 s13, 2
	s_cselect_b32 s59, s51, s59
	s_lshl_b32 s52, s59, 11
	s_add_u32 s46, s16, s52
	s_addc_u32 s47, s17, 0
	s_lshl_b32 s52, s6, 13
	s_mov_b32 m0, s52
	s_add_i32 s52, s52, 0x400
	global_load_lds_dwordx4 v211, s[46:47]
	s_mov_b32 m0, s52
	s_add_i32 s52, s52, 0x400
	global_load_lds_dwordx4 v212, s[46:47]
	s_mov_b32 m0, s52
	s_add_i32 s52, s52, 0x400
	global_load_lds_dwordx4 v213, s[46:47]
	s_mov_b32 m0, s52
	s_add_i32 s52, s52, 0x400
	global_load_lds_dwordx4 v214, s[46:47]
	s_mov_b32 m0, s52
	s_add_i32 s52, s52, 0x400
	global_load_lds_dwordx4 v215, s[46:47]
	s_mov_b32 m0, s52
	s_add_i32 s52, s52, 0x400
	global_load_lds_dwordx4 v216, s[46:47]
	s_mov_b32 m0, s52
	s_add_i32 s52, s52, 0x400
	global_load_lds_dwordx4 v217, s[46:47]
	s_mov_b32 m0, s52
	s_nop 0
	global_load_lds_dwordx4 v218, s[46:47]
	s_waitcnt vmcnt(8)
	v_mul_f32_e32 v173, s53, v173
	v_mul_f32_e32 v174, s53, v174
	v_mul_f32_e32 v175, s53, v175
	v_exp_f32_e32 v175, v175
	s_nop 0
	v_add_f32_e32 v180, 1.0, v175
	v_log_f32_e32 v180, v180
	v_mov_b32_e32 v181, 0x3eaaaaab
	v_fma_f32 v181, v175, v181, -0.5
	v_fma_f32 v181, v175, v181, 1.0
	v_mul_f32_e32 v181, v175, v181
	v_mul_f32_e32 v181, 0x3fb8aa3b, v181
	v_cmp_gt_f32_e32 vcc, 0x3cf5c28f, v175
	s_nop 1
	v_cndmask_b32_e32 v175, v180, v181, vcc
	v_mul_f32_e32 v175, 0xc1000000, v175
	s_waitcnt vmcnt(0)
	s_barrier
	s_cmp_eq_u32 s13, 17
	s_cbranch_scc1 .Lmylru_nodma_1
	s_add_i32 s58, s13, 1
	s_cmp_lt_u32 s58, 2
	s_lshl_b32 s50, s58, 7
	s_lshl_b32 s51, s9, 8
	s_add_i32 s51, s51, 0x8000
	s_add_i32 s51, s51, s50
	s_lshl_b32 s59, s9, 11
	s_add_i32 s59, s59, s50
	s_addk_i32 s59, 0xff00
	s_cmp_lt_u32 s58, 2
	s_cselect_b32 s59, s51, s59
	s_lshl_b32 s52, s59, 11
	s_add_u32 s46, s16, s52
	s_addc_u32 s47, s17, 0
	s_lshl_b32 s52, s6, 13
	s_add_i32 s52, s52, 0x10000
	s_mov_b32 m0, s52
	s_add_i32 s52, s52, 0x400
	global_load_lds_dwordx4 v211, s[46:47]
	s_mov_b32 m0, s52
	s_add_i32 s52, s52, 0x400
	global_load_lds_dwordx4 v212, s[46:47]
	s_mov_b32 m0, s52
	s_add_i32 s52, s52, 0x400
	global_load_lds_dwordx4 v213, s[46:47]
	s_mov_b32 m0, s52
	s_add_i32 s52, s52, 0x400
	global_load_lds_dwordx4 v214, s[46:47]
	s_mov_b32 m0, s52
	s_add_i32 s52, s52, 0x400
	global_load_lds_dwordx4 v215, s[46:47]
	s_mov_b32 m0, s52
	s_add_i32 s52, s52, 0x400
	global_load_lds_dwordx4 v216, s[46:47]
	s_mov_b32 m0, s52
	s_add_i32 s52, s52, 0x400
	global_load_lds_dwordx4 v217, s[46:47]
	s_mov_b32 m0, s52
	s_nop 0
	global_load_lds_dwordx4 v218, s[46:47]

.Lmylru_w1_8:
	v_lshlrev_b32_e32 v178, 16, v247
	v_add_f32_e32 v144, v144, v178
	v_lshlrev_b32_e32 v128, 16, v128
	v_mul_f32_e32 v144, v144, v128
	v_cvt_pk_bf16_f32 v144, v144, v144
	v_and_b32_e32 v179, 0xffff0000, v247
	v_add_f32_e32 v145, v145, v179
	v_lshlrev_b32_e32 v129, 16, v129
	v_mul_f32_e32 v145, v145, v129
	v_cvt_pk_bf16_f32 v145, v145, v145
	v_lshlrev_b32_e32 v180, 16, v248
	v_add_f32_e32 v146, v146, v180
	v_lshlrev_b32_e32 v130, 16, v130
	v_mul_f32_e32 v146, v146, v130
	v_cvt_pk_bf16_f32 v146, v146, v146
	v_and_b32_e32 v181, 0xffff0000, v248
	v_add_f32_e32 v147, v147, v181
	v_lshlrev_b32_e32 v131, 16, v131
	v_mul_f32_e32 v147, v147, v131
	v_cvt_pk_bf16_f32 v147, v147, v147
	v_lshlrev_b32_e32 v178, 16, v249
	v_add_f32_e32 v148, v148, v178
	v_lshlrev_b32_e32 v132, 16, v132
	v_mul_f32_e32 v148, v148, v132
	v_cvt_pk_bf16_f32 v148, v148, v148
	v_and_b32_e32 v179, 0xffff0000, v249
	v_add_f32_e32 v149, v149, v179
	v_lshlrev_b32_e32 v133, 16, v133
	v_mul_f32_e32 v149, v149, v133
	v_cvt_pk_bf16_f32 v149, v149, v149
	v_lshlrev_b32_e32 v180, 16, v250
	v_add_f32_e32 v150, v150, v180
	v_lshlrev_b32_e32 v134, 16, v134
	v_mul_f32_e32 v150, v150, v134
	v_cvt_pk_bf16_f32 v150, v150, v150
	v_and_b32_e32 v181, 0xffff0000, v250
	v_add_f32_e32 v151, v151, v181
	v_lshlrev_b32_e32 v135, 16, v135
	v_mul_f32_e32 v151, v151, v135
	v_cvt_pk_bf16_f32 v151, v151, v151
	v_lshlrev_b32_e32 v178, 16, v251
	v_add_f32_e32 v152, v152, v178
	v_lshlrev_b32_e32 v136, 16, v136
	v_mul_f32_e32 v152, v152, v136
	v_cvt_pk_bf16_f32 v152, v152, v152
	v_and_b32_e32 v179, 0xffff0000, v251
	v_add_f32_e32 v153, v153, v179
	v_lshlrev_b32_e32 v137, 16, v137
	v_mul_f32_e32 v153, v153, v137
	v_cvt_pk_bf16_f32 v153, v153, v153
	v_lshlrev_b32_e32 v180, 16, v252
	v_add_f32_e32 v154, v154, v180
	v_lshlrev_b32_e32 v138, 16, v138
	v_mul_f32_e32 v154, v154, v138
	v_cvt_pk_bf16_f32 v154, v154, v154
	v_and_b32_e32 v181, 0xffff0000, v252
	v_add_f32_e32 v155, v155, v181
	v_lshlrev_b32_e32 v139, 16, v139
	v_mul_f32_e32 v155, v155, v139
	v_cvt_pk_bf16_f32 v155, v155, v155
	v_lshlrev_b32_e32 v178, 16, v253
	v_add_f32_e32 v156, v156, v178
	v_lshlrev_b32_e32 v140, 16, v140
	v_mul_f32_e32 v156, v156, v140
	v_cvt_pk_bf16_f32 v156, v156, v156
	v_and_b32_e32 v179, 0xffff0000, v253
	v_add_f32_e32 v157, v157, v179
	v_lshlrev_b32_e32 v141, 16, v141
	v_mul_f32_e32 v157, v157, v141
	v_cvt_pk_bf16_f32 v157, v157, v157
	v_lshlrev_b32_e32 v180, 16, v254
	v_add_f32_e32 v158, v158, v180
	v_lshlrev_b32_e32 v142, 16, v142
	v_mul_f32_e32 v158, v158, v142
	v_cvt_pk_bf16_f32 v158, v158, v158
	v_and_b32_e32 v181, 0xffff0000, v254
	v_add_f32_e32 v159, v159, v181
	v_lshlrev_b32_e32 v143, 16, v143
	v_mul_f32_e32 v159, v159, v143
	v_cvt_pk_bf16_f32 v159, v159, v159
	v_add_u32_e32 v182, 0x0, v210
	v_add_u32_e32 v183, 0x1000, v182
	global_store_short v182, v144, s[42:43]
	global_store_short v182, v145, s[42:43] offset:2048
	global_store_short v183, v146, s[42:43]
	global_store_short v183, v147, s[42:43] offset:2048
	v_add_u32_e32 v182, 0x8000, v210
	v_add_u32_e32 v183, 0x1000, v182
	global_store_short v182, v148, s[42:43]
	global_store_short v182, v149, s[42:43] offset:2048
	global_store_short v183, v150, s[42:43]
	global_store_short v183, v151, s[42:43] offset:2048
	v_add_u32_e32 v182, 0x10000, v210
	v_add_u32_e32 v183, 0x1000, v182
	global_store_short v182, v152, s[42:43]
	global_store_short v182, v153, s[42:43] offset:2048
	global_store_short v183, v154, s[42:43]
	global_store_short v183, v155, s[42:43] offset:2048
	v_add_u32_e32 v182, 0x18000, v210
	v_add_u32_e32 v183, 0x1000, v182
	global_store_short v182, v156, s[42:43]
	global_store_short v182, v157, s[42:43] offset:2048
	global_store_short v183, v158, s[42:43]
	global_store_short v183, v159, s[42:43] offset:2048
	s_add_i32 s13, s13, 1
	s_add_i32 s60, s60, -1
	s_cmp_lg_u32 s60, 0
	s_cbranch_scc1 .Lmylru_loop_1
	s_waitcnt vmcnt(0) lgkmcnt(0)
	s_setprio 0
